# speedup vs baseline: 1.0163x; 1.0163x over previous
.LBB8_6:
	s_endpgm
	s_endpgm
	s_endpgm
	s_endpgm
	s_endpgm
	s_endpgm
	s_endpgm
	s_endpgm
	s_endpgm
	s_endpgm
	s_endpgm
	s_endpgm
	s_endpgm
	s_endpgm
	s_endpgm
	s_endpgm
	s_endpgm
	s_endpgm
	s_endpgm
	s_endpgm
	s_endpgm
	s_endpgm
	s_endpgm
	s_endpgm
	s_endpgm
	s_endpgm
	s_endpgm
	s_endpgm
	s_endpgm
	s_endpgm
	s_endpgm
	s_endpgm
	s_endpgm
	s_endpgm
	s_endpgm
	s_endpgm
	s_endpgm
	s_endpgm
	s_endpgm
	s_endpgm
	s_endpgm
	s_endpgm
	s_endpgm
	s_endpgm
	s_endpgm
	s_endpgm
	s_endpgm
	s_endpgm
	s_endpgm

.LBB9_1:
	s_waitcnt lgkmcnt(0)
	v_mfma_f32_32x32x16_f16 v[112:127], v[148:151], v[136:139], v[112:127]
	s_mov_b32 s14, 1
	s_mov_b64 s[34:35], 0
	s_and_b64 vcc, exec, s[30:31]
	v_mfma_f32_32x32x16_f16 v[96:111], v[144:147], v[136:139], v[96:111]
	s_nop 7
	v_fma_f32 v112, v236, v112, v235
	v_fma_f32 v113, v236, v113, v235
	v_fma_f32 v114, v236, v114, v235
	v_fma_f32 v115, v236, v115, v235
	v_max_f32_e32 v112, v112, v113
	v_max_f32_e32 v113, v114, v115
	v_max3_f32 v112, v112, v113, 0
	v_mfma_f32_32x32x16_f16 v[80:95], v[140:143], v[136:139], v[80:95]
	v_cvt_f16_f32_e32 v112, v112
	v_fma_f32 v116, v236, v116, v235
	v_fma_f32 v117, v236, v117, v235
	v_fma_f32 v118, v236, v118, v235
	v_fma_f32 v113, v236, v119, v235
	v_fma_f32 v96, v236, v96, v235
	v_fma_f32 v97, v236, v97, v235
	v_mfma_f32_32x32x16_f16 v[48:63], v[128:131], v[136:139], v[48:63]
	v_fma_f32 v98, v236, v98, v235
	v_fma_f32 v99, v236, v99, v235
	s_nop 1
	v_fma_f32 v80, v236, v80, v235
	v_fma_f32 v81, v236, v81, v235
	v_fma_f32 v82, v236, v82, v235
	v_fma_f32 v83, v236, v83, v235
	v_max_f32_e32 v114, v116, v117
	s_nop 2
	v_fma_f32 v48, v236, v48, v235
	v_fma_f32 v49, v236, v49, v235
	v_fma_f32 v50, v236, v50, v235
	v_fma_f32 v51, v236, v51, v235
	ds_write_b16 v232, v112
	v_max_f32_e32 v112, v118, v113
	v_max_f32_e32 v96, v96, v97
	v_max_f32_e32 v97, v98, v99
	v_max_f32_e32 v80, v80, v81
	v_max_f32_e32 v81, v82, v83
	v_max_f32_e32 v48, v48, v49
	v_max_f32_e32 v49, v50, v51
	v_mfma_f32_32x32x16_f16 v[64:79], v[148:151], v[132:135], v[64:79]
	v_max3_f32 v112, v114, v112, 0
	v_fma_f32 v113, v236, v120, v235
	v_fma_f32 v114, v236, v121, v235
	v_fma_f32 v115, v236, v122, v235
	v_fma_f32 v116, v236, v123, v235
	v_max3_f32 v96, v96, v97, 0
	v_fma_f32 v97, v236, v100, v235
	v_mfma_f32_32x32x16_f16 v[32:47], v[144:147], v[132:135], v[32:47]
	v_fma_f32 v98, v236, v101, v235
	v_fma_f32 v99, v236, v102, v235
	v_fma_f32 v100, v236, v103, v235
	v_max3_f32 v80, v80, v81, 0
	v_fma_f32 v81, v236, v84, v235
	v_fma_f32 v82, v236, v85, v235
	v_fma_f32 v83, v236, v86, v235
	v_mfma_f32_32x32x16_f16 v[16:31], v[140:143], v[132:135], v[16:31]
	v_fma_f32 v84, v236, v87, v235
	v_max3_f32 v48, v48, v49, 0
	v_fma_f32 v49, v236, v52, v235
	v_fma_f32 v50, v236, v53, v235
	v_fma_f32 v51, v236, v54, v235
	v_fma_f32 v52, v236, v55, v235
	v_max_f32_e32 v113, v113, v114
	v_mfma_f32_32x32x16_f16 v[0:15], v[128:131], v[132:135], v[0:15]
	v_max_f32_e32 v114, v115, v116
	v_max_f32_e32 v97, v97, v98
	v_max_f32_e32 v98, v99, v100
	v_max_f32_e32 v81, v81, v82
	v_max_f32_e32 v82, v83, v84
	v_max_f32_e32 v49, v49, v50
	v_max_f32_e32 v50, v51, v52
	v_max3_f32 v113, v113, v114, 0
	v_fma_f32 v114, v236, v124, v235
	v_fma_f32 v115, v236, v125, v235
	v_fma_f32 v116, v236, v126, v235
	v_fma_f32 v117, v236, v127, v235
	v_max3_f32 v97, v97, v98, 0
	v_fma_f32 v98, v236, v104, v235
	v_fma_f32 v99, v236, v105, v235
	v_fma_f32 v100, v236, v106, v235
	v_fma_f32 v101, v236, v107, v235
	v_max3_f32 v81, v81, v82, 0
	v_fma_f32 v82, v236, v88, v235
	v_fma_f32 v83, v236, v89, v235
	v_fma_f32 v84, v236, v90, v235
	v_fma_f32 v85, v236, v91, v235
	v_max3_f32 v49, v49, v50, 0
	v_fma_f32 v50, v236, v56, v235
	v_fma_f32 v51, v236, v57, v235
	v_fma_f32 v52, v236, v58, v235
	v_fma_f32 v53, v236, v59, v235
	v_max_f32_e32 v114, v114, v115
	v_max_f32_e32 v115, v116, v117
	v_max_f32_e32 v98, v98, v99
	v_max_f32_e32 v99, v100, v101
	v_max_f32_e32 v82, v82, v83
	v_max_f32_e32 v83, v84, v85
	v_max_f32_e32 v50, v50, v51
	v_max_f32_e32 v51, v52, v53
	v_cvt_f16_f32_e32 v112, v112
	v_cvt_f16_f32_e32 v113, v113
	v_max3_f32 v114, v114, v115, 0
	v_cvt_f16_f32_e32 v96, v96
	v_max3_f32 v98, v98, v99, 0
	v_fma_f32 v99, v236, v108, v235
	v_fma_f32 v100, v236, v109, v235
	v_fma_f32 v101, v236, v110, v235
	v_fma_f32 v102, v236, v111, v235
	v_cvt_f16_f32_e32 v80, v80
	v_max3_f32 v82, v82, v83, 0
	v_fma_f32 v83, v236, v92, v235
	v_fma_f32 v84, v236, v93, v235
	v_fma_f32 v85, v236, v94, v235
	v_fma_f32 v86, v236, v95, v235
	v_cvt_f16_f32_e32 v48, v48
	v_max3_f32 v50, v50, v51, 0
	v_fma_f32 v51, v236, v60, v235
	v_fma_f32 v52, v236, v61, v235
	v_fma_f32 v53, v236, v62, v235
	v_fmac_f32_e32 v235, v236, v63
	v_cvt_f16_f32_e32 v114, v114
	v_cvt_f16_f32_e32 v97, v97
	v_max_f32_e32 v99, v99, v100
	v_max_f32_e32 v100, v101, v102
	v_cvt_f16_f32_e32 v81, v81
	v_max_f32_e32 v83, v83, v84
	v_max_f32_e32 v84, v85, v86
	v_cvt_f16_f32_e32 v49, v49
	v_max_f32_e32 v51, v51, v52
	v_max_f32_e32 v52, v53, v235
	v_cvt_f16_f32_e32 v98, v98
	v_max3_f32 v99, v99, v100, 0
	v_cvt_f16_f32_e32 v82, v82
	v_max3_f32 v83, v83, v84, 0
	v_cvt_f16_f32_e32 v50, v50
	v_max3_f32 v51, v51, v52, 0
	v_cvt_f16_f32_e32 v99, v99
	v_cvt_f16_f32_e32 v83, v83
	v_cvt_f16_f32_e32 v51, v51
	ds_write_b16 v232, v112 offset:512
	ds_write_b16 v232, v113 offset:1024
	ds_write_b16 v232, v114 offset:1536
	ds_write_b16 v232, v96 offset:2048
	ds_write_b16 v232, v97 offset:2560
	ds_write_b16 v232, v98 offset:3072
	ds_write_b16 v232, v99 offset:3584
	ds_write_b16 v232, v80 offset:4096
	ds_write_b16 v232, v81 offset:4608
	ds_write_b16 v232, v82 offset:5120
	ds_write_b16 v232, v83 offset:5632
	ds_write_b16 v232, v48 offset:6144
	ds_write_b16 v232, v49 offset:6656
	ds_write_b16 v232, v50 offset:7168
	ds_write_b16 v232, v51 offset:7680
	v_fma_f32 v48, v234, v64, v233
	v_fma_f32 v49, v234, v65, v233
	v_fma_f32 v50, v234, v66, v233
	v_fma_f32 v51, v234, v67, v233
	v_fma_f32 v32, v234, v32, v233
	v_fma_f32 v33, v234, v33, v233
	v_fma_f32 v34, v234, v34, v233
	v_fma_f32 v35, v234, v35, v233
	v_fma_f32 v16, v234, v16, v233
	v_fma_f32 v17, v234, v17, v233
	v_fma_f32 v18, v234, v18, v233
	v_fma_f32 v19, v234, v19, v233
	v_fma_f32 v0, v234, v0, v233
	v_fma_f32 v1, v234, v1, v233
	v_fma_f32 v2, v234, v2, v233
	v_fma_f32 v3, v234, v3, v233
	v_max_f32_e32 v48, v48, v49
	v_max_f32_e32 v49, v50, v51
	v_max_f32_e32 v32, v32, v33
	v_max_f32_e32 v33, v34, v35
	v_max_f32_e32 v16, v16, v17
	v_max_f32_e32 v17, v18, v19
	v_max_f32_e32 v0, v0, v1
	v_max_f32_e32 v1, v2, v3
	v_max3_f32 v48, v48, v49, 0
	v_fma_f32 v49, v234, v68, v233
	v_fma_f32 v50, v234, v69, v233
	v_fma_f32 v51, v234, v70, v233
	v_fma_f32 v52, v234, v71, v233
	v_max3_f32 v32, v32, v33, 0
	v_fma_f32 v33, v234, v36, v233
	v_fma_f32 v34, v234, v37, v233
	v_fma_f32 v35, v234, v38, v233
	v_fma_f32 v36, v234, v39, v233
	v_max3_f32 v16, v16, v17, 0
	v_fma_f32 v17, v234, v20, v233
	v_fma_f32 v18, v234, v21, v233
	v_fma_f32 v19, v234, v22, v233
	v_fma_f32 v20, v234, v23, v233
	v_max3_f32 v0, v0, v1, 0
	v_fma_f32 v1, v234, v4, v233
	v_fma_f32 v2, v234, v5, v233
	v_fma_f32 v3, v234, v6, v233
	v_fma_f32 v4, v234, v7, v233
	v_max_f32_e32 v49, v49, v50
	v_max_f32_e32 v50, v51, v52
	v_max_f32_e32 v33, v33, v34
	v_max_f32_e32 v34, v35, v36
	v_max_f32_e32 v17, v17, v18
	v_max_f32_e32 v18, v19, v20
	v_max_f32_e32 v1, v1, v2
	v_max_f32_e32 v2, v3, v4
	v_max3_f32 v49, v49, v50, 0
	v_fma_f32 v50, v234, v72, v233
	v_fma_f32 v51, v234, v73, v233
	v_fma_f32 v52, v234, v74, v233
	v_fma_f32 v53, v234, v75, v233
	v_max3_f32 v33, v33, v34, 0
	v_fma_f32 v34, v234, v40, v233
	v_fma_f32 v35, v234, v41, v233
	v_fma_f32 v36, v234, v42, v233
	v_fma_f32 v37, v234, v43, v233
	v_max3_f32 v17, v17, v18, 0
	v_fma_f32 v18, v234, v24, v233
	v_fma_f32 v19, v234, v25, v233
	v_fma_f32 v20, v234, v26, v233
	v_fma_f32 v21, v234, v27, v233
	v_max3_f32 v1, v1, v2, 0
	v_fma_f32 v2, v234, v8, v233
	v_fma_f32 v3, v234, v9, v233
	v_fma_f32 v4, v234, v10, v233
	v_fma_f32 v5, v234, v11, v233
	v_max_f32_e32 v50, v50, v51
	v_max_f32_e32 v51, v52, v53
	v_max_f32_e32 v34, v34, v35
	v_max_f32_e32 v35, v36, v37
	v_max_f32_e32 v18, v18, v19
	v_max_f32_e32 v19, v20, v21
	v_max_f32_e32 v2, v2, v3
	v_max_f32_e32 v3, v4, v5
	v_cvt_f16_f32_e32 v48, v48
	v_max3_f32 v50, v50, v51, 0
	v_fma_f32 v51, v234, v76, v233
	v_fma_f32 v52, v234, v77, v233
	v_fma_f32 v53, v234, v78, v233
	v_fma_f32 v54, v234, v79, v233
	v_cvt_f16_f32_e32 v32, v32
	v_max3_f32 v34, v34, v35, 0
	v_fma_f32 v35, v234, v44, v233
	v_fma_f32 v36, v234, v45, v233
	v_fma_f32 v37, v234, v46, v233
	v_fma_f32 v38, v234, v47, v233
	v_cvt_f16_f32_e32 v16, v16
	v_max3_f32 v18, v18, v19, 0
	v_fma_f32 v19, v234, v28, v233
	v_fma_f32 v20, v234, v29, v233
	v_fma_f32 v21, v234, v30, v233
	v_fma_f32 v22, v234, v31, v233
	v_cvt_f16_f32_e32 v0, v0
	v_max3_f32 v2, v2, v3, 0
	v_fma_f32 v3, v234, v12, v233
	v_fma_f32 v4, v234, v13, v233
	v_fma_f32 v5, v234, v14, v233
	v_fmac_f32_e32 v233, v234, v15
	v_cvt_f16_f32_e32 v49, v49
	v_max_f32_e32 v51, v51, v52
	v_max_f32_e32 v52, v53, v54
	v_cvt_f16_f32_e32 v33, v33
	v_max_f32_e32 v35, v35, v36
	v_max_f32_e32 v36, v37, v38
	v_cvt_f16_f32_e32 v17, v17
	v_max_f32_e32 v19, v19, v20
	v_max_f32_e32 v20, v21, v22
	v_cvt_f16_f32_e32 v1, v1
	v_max_f32_e32 v3, v3, v4
	v_max_f32_e32 v4, v5, v233
	v_cvt_f16_f32_e32 v50, v50
	v_max3_f32 v51, v51, v52, 0
	v_cvt_f16_f32_e32 v34, v34
	v_max3_f32 v35, v35, v36, 0
	v_cvt_f16_f32_e32 v18, v18
	v_max3_f32 v19, v19, v20, 0
	v_cvt_f16_f32_e32 v2, v2
	v_max3_f32 v3, v3, v4, 0
	v_cvt_f16_f32_e32 v51, v51
	v_cvt_f16_f32_e32 v35, v35
	v_cvt_f16_f32_e32 v19, v19
	v_cvt_f16_f32_e32 v3, v3
	ds_write_b16 v232, v48 offset:64
	ds_write_b16 v232, v49 offset:576
	ds_write_b16 v232, v50 offset:1088
	ds_write_b16 v232, v51 offset:1600
	ds_write_b16 v232, v32 offset:2112
	ds_write_b16 v232, v33 offset:2624
	ds_write_b16 v232, v34 offset:3136
	ds_write_b16 v232, v35 offset:3648
	ds_write_b16 v232, v16 offset:4160
	ds_write_b16 v232, v17 offset:4672
	ds_write_b16 v232, v18 offset:5184
	ds_write_b16 v232, v19 offset:5696
	ds_write_b16 v232, v0 offset:6208
	ds_write_b16 v232, v1 offset:6720
	ds_write_b16 v232, v2 offset:7232
	ds_write_b16 v232, v3 offset:7744
	s_waitcnt vmcnt(0) lgkmcnt(0)
	s_barrier
	v_lshl_or_b32 v10, s49, 3, v224
	ds_read_b128 v[0:3], v225
	v_or_b32_e32 v4, v184, v10
	v_mov_b32_e32 v5, v185
	v_lshlrev_b64 v[4:5], 8, v[4:5]
	v_lshl_add_u64 v[8:9], v[186:187], 0, v[4:5]
	ds_read_b128 v[4:7], v226
	s_waitcnt lgkmcnt(1)
	global_store_dwordx4 v[8:9], v[0:3], off sc0 sc1
	s_nop 1
	v_or_b32_e32 v0, v188, v10
	v_mov_b32_e32 v1, v189
	v_lshlrev_b64 v[0:1], 8, v[0:1]
	v_lshl_add_u64 v[0:1], v[186:187], 0, v[0:1]
	s_waitcnt lgkmcnt(0)
	global_store_dwordx4 v[0:1], v[4:7], off sc0 sc1
	ds_read_b128 v[0:3], v227
	s_nop 0
	v_or_b32_e32 v4, v190, v10
	v_mov_b32_e32 v5, v191
	v_lshlrev_b64 v[4:5], 8, v[4:5]
	v_lshl_add_u64 v[8:9], v[186:187], 0, v[4:5]
	ds_read_b128 v[4:7], v228
	s_waitcnt lgkmcnt(1)
	global_store_dwordx4 v[8:9], v[0:3], off sc0 sc1
	s_nop 1
	v_or_b32_e32 v0, v192, v10
	v_mov_b32_e32 v1, v193
	v_lshlrev_b64 v[0:1], 8, v[0:1]
	v_lshl_add_u64 v[0:1], v[186:187], 0, v[0:1]
	s_waitcnt lgkmcnt(0)
	global_store_dwordx4 v[0:1], v[4:7], off sc0 sc1
	s_cbranch_vccnz .LBB9_31

.LBB9_31:
	s_endpgm
	s_endpgm
	s_endpgm
	s_endpgm
	s_endpgm
	s_endpgm
	s_endpgm
	s_endpgm
	s_endpgm
	s_endpgm
	s_endpgm
	s_endpgm
	s_endpgm
	s_endpgm
	s_endpgm
	s_endpgm
	s_endpgm
	s_endpgm
	s_endpgm
	s_endpgm
	s_endpgm
	s_endpgm
	s_endpgm
	s_endpgm
	s_endpgm
	s_endpgm
	s_endpgm
	s_endpgm
	s_endpgm
	s_endpgm
	s_endpgm
	s_endpgm
	s_endpgm
	s_endpgm
	s_endpgm
	s_endpgm
	s_endpgm
	s_endpgm
	s_endpgm
	s_endpgm
	s_endpgm
	s_endpgm
	s_endpgm
	s_endpgm
	s_endpgm
	s_endpgm
	s_endpgm
	s_endpgm
	s_endpgm
	s_endpgm
	s_endpgm
	s_endpgm
	s_endpgm
	s_endpgm
	s_endpgm
	s_endpgm

.LBB10_8:
	s_waitcnt lgkmcnt(0)
	v_mfma_f32_32x32x16_f16 v[66:81], v[170:173], v[174:177], v[66:81]
	v_or_b32_e32 v1, 0x600, v0
	v_lshrrev_b32_e32 v178, 3, v1
	s_lshl_b32 s4, s13, 8
	v_and_b32_e32 v178, 0xe0, v178
	v_bfe_u32 v179, v0, 5, 3
	s_lshl_b64 s[2:3], s[2:3], 10
	v_or_b32_e32 v178, s4, v178
	v_mfma_f32_32x32x16_f16 v[66:81], v[150:153], v[146:149], v[66:81]
	v_lshl_or_b32 v183, s12, 3, v179
	v_or3_b32 v180, s2, v178, v183
	v_mov_b32_e32 v181, s3
	v_lshlrev_b64 v[178:179], 9, v[180:181]
	v_lshlrev_b32_e32 v1, 4, v1
	s_movk_i32 s3, 0x7e00
	v_lshl_add_u64 v[178:179], s[0:1], 0, v[178:179]
	v_mfma_f32_32x32x16_f16 v[82:97], v[162:165], v[174:177], v[82:97]
	s_nop 3
	v_fma_f32 v66, v221, v66, v220
	v_fma_f32 v67, v221, v67, v220
	v_fma_f32 v68, v221, v68, v220
	v_fma_f32 v69, v221, v69, v220
	v_max_f32_e32 v66, v66, v67
	v_max_f32_e32 v67, v68, v69
	v_max3_f32 v66, v66, v67, 0
	v_fma_f32 v67, v221, v70, v220
	v_fma_f32 v68, v221, v71, v220
	v_fma_f32 v69, v221, v72, v220
	v_fma_f32 v70, v221, v73, v220
	v_mfma_f32_32x32x16_f16 v[82:97], v[138:141], v[146:149], v[82:97]
	v_max_f32_e32 v67, v67, v68
	v_max_f32_e32 v68, v69, v70
	v_max3_f32 v67, v67, v68, 0
	v_fma_f32 v68, v221, v74, v220
	v_fma_f32 v69, v221, v75, v220
	v_fma_f32 v70, v221, v76, v220
	v_fma_f32 v71, v221, v77, v220
	v_mfma_f32_32x32x16_f16 v[114:129], v[158:161], v[174:177], v[114:129]
	v_max_f32_e32 v68, v68, v69
	v_max_f32_e32 v69, v70, v71
	v_cvt_f16_f32_e32 v66, v66
	v_max3_f32 v68, v68, v69, 0
	v_fma_f32 v69, v221, v78, v220
	v_fma_f32 v70, v221, v79, v220
	v_fma_f32 v71, v221, v80, v220
	v_mfma_f32_32x32x16_f16 v[50:65], v[158:161], v[166:169], v[50:65]
	v_lshlrev_b32_e32 v159, 1, v219
	v_fma_f32 v72, v221, v81, v220
	v_lshl_add_u32 v159, v218, 1, v159
	v_cvt_f16_f32_e32 v67, v67
	v_max_f32_e32 v69, v69, v70
	v_max_f32_e32 v70, v71, v72
	v_lshl_or_b32 v159, v222, 14, v159
	v_cvt_f16_f32_e32 v68, v68
	v_max3_f32 v69, v69, v70, 0
	v_lshl_add_u32 v159, v223, 9, v159
	v_cvt_f16_f32_e32 v69, v69
	ds_write_b16 v159, v66
	ds_write_b16 v159, v67 offset:1024
	ds_write_b16 v159, v68 offset:2048
	ds_write_b16 v159, v69 offset:3072
	v_fma_f32 v66, v221, v82, v220
	v_fma_f32 v67, v221, v83, v220
	v_fma_f32 v68, v221, v84, v220
	v_fma_f32 v69, v221, v85, v220
	v_max_f32_e32 v66, v66, v67
	v_max_f32_e32 v67, v68, v69
	v_mfma_f32_32x32x16_f16 v[114:129], v[134:137], v[146:149], v[114:129]
	v_max3_f32 v66, v66, v67, 0
	v_fma_f32 v67, v221, v86, v220
	v_fma_f32 v68, v221, v87, v220
	v_fma_f32 v69, v221, v88, v220
	v_fma_f32 v70, v221, v89, v220
	v_max_f32_e32 v67, v67, v68
	v_max_f32_e32 v68, v69, v70
	v_mfma_f32_32x32x16_f16 v[34:49], v[170:173], v[166:169], v[34:49]
	v_max3_f32 v67, v67, v68, 0
	v_fma_f32 v68, v221, v90, v220
	v_fma_f32 v69, v221, v91, v220
	v_fma_f32 v70, v221, v92, v220
	v_fma_f32 v71, v221, v93, v220
	v_max_f32_e32 v68, v68, v69
	v_max_f32_e32 v69, v70, v71
	v_mfma_f32_32x32x16_f16 v[2:17], v[162:165], v[166:169], v[2:17]
	v_cvt_f16_f32_e32 v66, v66
	v_max3_f32 v68, v68, v69, 0
	v_fma_f32 v69, v221, v94, v220
	v_fma_f32 v70, v221, v95, v220
	v_fma_f32 v71, v221, v96, v220
	v_fma_f32 v72, v221, v97, v220
	v_cvt_f16_f32_e32 v67, v67
	v_mfma_f32_32x32x16_f16 v[98:113], v[154:157], v[174:177], v[98:113]
	v_max_f32_e32 v69, v69, v70
	v_max_f32_e32 v70, v71, v72
	v_cvt_f16_f32_e32 v68, v68
	v_max3_f32 v69, v69, v70, 0
	v_cvt_f16_f32_e32 v69, v69
	ds_write_b16 v159, v66 offset:4096
	ds_write_b16 v159, v67 offset:5120
	ds_write_b16 v159, v68 offset:6144
	ds_write_b16 v159, v69 offset:7168
	v_fma_f32 v66, v221, v114, v220
	v_fma_f32 v67, v221, v115, v220
	v_fma_f32 v68, v221, v116, v220
	v_fma_f32 v69, v221, v117, v220
	v_max_f32_e32 v66, v66, v67
	v_max_f32_e32 v67, v68, v69
	v_mfma_f32_32x32x16_f16 v[34:49], v[150:153], v[142:145], v[34:49]
	v_max3_f32 v66, v66, v67, 0
	v_fma_f32 v67, v221, v118, v220
	v_fma_f32 v68, v221, v119, v220
	v_fma_f32 v69, v221, v120, v220
	v_fma_f32 v70, v221, v121, v220
	v_max_f32_e32 v67, v67, v68
	v_max_f32_e32 v68, v69, v70
	v_mfma_f32_32x32x16_f16 v[2:17], v[138:141], v[142:145], v[2:17]
	v_max3_f32 v67, v67, v68, 0
	v_fma_f32 v68, v221, v122, v220
	v_fma_f32 v69, v221, v123, v220
	v_fma_f32 v70, v221, v124, v220
	v_fma_f32 v71, v221, v125, v220
	v_max_f32_e32 v68, v68, v69
	v_max_f32_e32 v69, v70, v71
	v_mfma_f32_32x32x16_f16 v[98:113], v[130:133], v[146:149], v[98:113]
	v_cvt_f16_f32_e32 v66, v66
	v_max3_f32 v68, v68, v69, 0
	v_fma_f32 v69, v221, v126, v220
	v_fma_f32 v70, v221, v127, v220
	v_fma_f32 v71, v221, v128, v220
	v_fma_f32 v72, v221, v129, v220
	v_cvt_f16_f32_e32 v67, v67
	v_max_f32_e32 v69, v69, v70
	v_max_f32_e32 v70, v71, v72
	v_cvt_f16_f32_e32 v68, v68
	v_max3_f32 v69, v69, v70, 0
	v_cvt_f16_f32_e32 v69, v69
	ds_write_b16 v159, v66 offset:8192
	ds_write_b16 v159, v67 offset:9216
	ds_write_b16 v159, v68 offset:10240
	ds_write_b16 v159, v69 offset:11264
	v_fma_f32 v66, v221, v98, v220
	v_fma_f32 v67, v221, v99, v220
	v_fma_f32 v68, v221, v100, v220
	v_fma_f32 v69, v221, v101, v220
	v_fma_f32 v34, v217, v34, v216
	v_fma_f32 v35, v217, v35, v216
	v_fma_f32 v36, v217, v36, v216
	v_fma_f32 v37, v217, v37, v216
	v_fma_f32 v2, v217, v2, v216
	v_fma_f32 v3, v217, v3, v216
	v_fma_f32 v4, v217, v4, v216
	v_fma_f32 v5, v217, v5, v216
	v_max_f32_e32 v66, v66, v67
	v_max_f32_e32 v67, v68, v69
	v_max_f32_e32 v34, v34, v35
	v_max_f32_e32 v35, v36, v37
	v_max_f32_e32 v2, v2, v3
	v_max_f32_e32 v3, v4, v5
	v_mfma_f32_32x32x16_f16 v[50:65], v[134:137], v[142:145], v[50:65]
	v_max3_f32 v66, v66, v67, 0
	v_fma_f32 v67, v221, v102, v220
	v_fma_f32 v68, v221, v103, v220
	v_fma_f32 v69, v221, v104, v220
	v_fma_f32 v70, v221, v105, v220
	v_max3_f32 v34, v34, v35, 0
	v_fma_f32 v35, v217, v38, v216
	v_fma_f32 v36, v217, v39, v216
	v_fma_f32 v37, v217, v40, v216
	v_fma_f32 v38, v217, v41, v216
	v_max3_f32 v2, v2, v3, 0
	v_fma_f32 v3, v217, v6, v216
	v_fma_f32 v4, v217, v7, v216
	v_fma_f32 v5, v217, v8, v216
	v_fma_f32 v6, v217, v9, v216
	v_max_f32_e32 v67, v67, v68
	v_max_f32_e32 v68, v69, v70
	v_max_f32_e32 v35, v35, v36
	v_max_f32_e32 v36, v37, v38
	v_max_f32_e32 v3, v3, v4
	v_max_f32_e32 v4, v5, v6
	v_mfma_f32_32x32x16_f16 v[18:33], v[154:157], v[166:169], v[18:33]
	v_max3_f32 v67, v67, v68, 0
	v_fma_f32 v68, v221, v106, v220
	v_fma_f32 v69, v221, v107, v220
	v_fma_f32 v70, v221, v108, v220
	v_fma_f32 v71, v221, v109, v220
	v_max3_f32 v35, v35, v36, 0
	v_fma_f32 v36, v217, v42, v216
	v_fma_f32 v37, v217, v43, v216
	v_fma_f32 v38, v217, v44, v216
	v_fma_f32 v39, v217, v45, v216
	v_max3_f32 v3, v3, v4, 0
	v_fma_f32 v4, v217, v10, v216
	v_fma_f32 v5, v217, v11, v216
	v_fma_f32 v6, v217, v12, v216
	v_fma_f32 v7, v217, v13, v216
	v_max_f32_e32 v68, v68, v69
	v_max_f32_e32 v69, v70, v71
	v_max_f32_e32 v36, v36, v37
	v_max_f32_e32 v37, v38, v39
	v_max_f32_e32 v4, v4, v5
	v_max_f32_e32 v5, v6, v7
	v_cvt_f16_f32_e32 v66, v66
	v_max3_f32 v68, v68, v69, 0
	v_fma_f32 v69, v221, v110, v220
	v_fma_f32 v70, v221, v111, v220
	v_fma_f32 v71, v221, v112, v220
	v_fmac_f32_e32 v220, v221, v113
	v_cvt_f16_f32_e32 v34, v34
	v_max3_f32 v36, v36, v37, 0
	v_fma_f32 v37, v217, v46, v216
	v_fma_f32 v38, v217, v47, v216
	v_fma_f32 v39, v217, v48, v216
	v_fma_f32 v40, v217, v49, v216
	v_cvt_f16_f32_e32 v2, v2
	v_max3_f32 v4, v4, v5, 0
	v_fma_f32 v5, v217, v14, v216
	v_fma_f32 v6, v217, v15, v216
	v_fma_f32 v7, v217, v16, v216
	v_fma_f32 v8, v217, v17, v216
	v_cvt_f16_f32_e32 v67, v67
	v_max_f32_e32 v69, v69, v70
	v_max_f32_e32 v70, v71, v220
	v_cvt_f16_f32_e32 v35, v35
	v_max_f32_e32 v37, v37, v38
	v_max_f32_e32 v38, v39, v40
	v_cvt_f16_f32_e32 v3, v3
	v_max_f32_e32 v5, v5, v6
	v_max_f32_e32 v6, v7, v8
	v_cvt_f16_f32_e32 v68, v68
	v_max3_f32 v69, v69, v70, 0
	v_cvt_f16_f32_e32 v36, v36
	v_max3_f32 v37, v37, v38, 0
	v_cvt_f16_f32_e32 v4, v4
	v_max3_f32 v5, v5, v6, 0
	v_cvt_f16_f32_e32 v69, v69
	v_cvt_f16_f32_e32 v37, v37
	v_cvt_f16_f32_e32 v5, v5
	ds_write_b16 v159, v66 offset:12288
	ds_write_b16 v159, v67 offset:13312
	ds_write_b16 v159, v68 offset:14336
	ds_write_b16 v159, v69 offset:15360
	ds_write_b16 v159, v34 offset:64
	ds_write_b16 v159, v35 offset:1088
	ds_write_b16 v159, v36 offset:2112
	ds_write_b16 v159, v37 offset:3136
	ds_write_b16 v159, v2 offset:4160
	ds_write_b16 v159, v3 offset:5184
	ds_write_b16 v159, v4 offset:6208
	ds_write_b16 v159, v5 offset:7232
	v_fma_f32 v2, v217, v50, v216
	v_fma_f32 v3, v217, v51, v216
	v_fma_f32 v4, v217, v52, v216
	v_fma_f32 v5, v217, v53, v216
	v_max_f32_e32 v2, v2, v3
	v_max_f32_e32 v3, v4, v5
	v_mfma_f32_32x32x16_f16 v[18:33], v[130:133], v[142:145], v[18:33]
	v_max3_f32 v2, v2, v3, 0
	v_fma_f32 v3, v217, v54, v216
	v_fma_f32 v4, v217, v55, v216
	v_fma_f32 v5, v217, v56, v216
	v_fma_f32 v6, v217, v57, v216
	v_max_f32_e32 v3, v3, v4
	v_max_f32_e32 v4, v5, v6
	v_max3_f32 v3, v3, v4, 0
	v_fma_f32 v4, v217, v58, v216
	v_fma_f32 v5, v217, v59, v216
	v_fma_f32 v6, v217, v60, v216
	v_fma_f32 v7, v217, v61, v216
	v_max_f32_e32 v4, v4, v5
	v_max_f32_e32 v5, v6, v7
	v_cvt_f16_f32_e32 v2, v2
	v_max3_f32 v4, v4, v5, 0
	v_fma_f32 v5, v217, v62, v216
	v_fma_f32 v6, v217, v63, v216
	v_fma_f32 v7, v217, v64, v216
	v_fma_f32 v8, v217, v65, v216
	v_cvt_f16_f32_e32 v3, v3
	v_max_f32_e32 v5, v5, v6
	v_max_f32_e32 v6, v7, v8
	v_cvt_f16_f32_e32 v4, v4
	v_max3_f32 v5, v5, v6, 0
	v_cvt_f16_f32_e32 v5, v5
	ds_write_b16 v159, v2 offset:8256
	ds_write_b16 v159, v3 offset:9280
	ds_write_b16 v159, v4 offset:10304
	ds_write_b16 v159, v5 offset:11328
	v_fma_f32 v2, v217, v18, v216
	v_fma_f32 v3, v217, v19, v216
	v_fma_f32 v4, v217, v20, v216
	v_fma_f32 v5, v217, v21, v216
	v_max_f32_e32 v2, v2, v3
	v_max_f32_e32 v3, v4, v5
	v_max3_f32 v2, v2, v3, 0
	v_fma_f32 v3, v217, v22, v216
	v_fma_f32 v4, v217, v23, v216
	v_fma_f32 v5, v217, v24, v216
	v_fma_f32 v6, v217, v25, v216
	v_lshlrev_b32_e32 v172, 4, v219
	v_max_f32_e32 v3, v3, v4
	v_max_f32_e32 v4, v5, v6
	v_mov_b32_e32 v173, 0
	v_and_or_b32 v184, v1, s3, v172
	v_or_b32_e32 v1, 0x400, v0
	v_max3_f32 v3, v3, v4, 0
	v_fma_f32 v4, v217, v26, v216
	v_fma_f32 v5, v217, v27, v216
	v_fma_f32 v6, v217, v28, v216
	v_fma_f32 v7, v217, v29, v216
	v_lshl_add_u64 v[170:171], v[178:179], 0, v[172:173]
	v_lshrrev_b32_e32 v178, 3, v1
	v_lshlrev_b32_e32 v1, 4, v1
	s_movk_i32 s3, 0x5e00
	v_max_f32_e32 v4, v4, v5
	v_max_f32_e32 v5, v6, v7
	v_and_or_b32 v164, v1, s3, v172
	v_or_b32_e32 v1, 0x200, v0
	v_cvt_f16_f32_e32 v2, v2
	v_max3_f32 v4, v4, v5, 0
	v_fma_f32 v5, v217, v30, v216
	v_fma_f32 v6, v217, v31, v216
	v_fma_f32 v7, v217, v32, v216
	v_fmac_f32_e32 v216, v217, v33
	v_and_b32_e32 v178, 0xa0, v178
	v_lshrrev_b32_e32 v162, 3, v1
	v_cvt_f16_f32_e32 v3, v3
	v_max_f32_e32 v5, v5, v6
	v_max_f32_e32 v6, v7, v216
	v_lshrrev_b32_e32 v182, 5, v0
	v_or_b32_e32 v178, s4, v178
	v_and_b32_e32 v162, 0x60, v162
	v_cvt_f16_f32_e32 v4, v4
	v_max3_f32 v5, v5, v6, 0
	v_or3_b32 v180, s2, v178, v183
	v_or_b32_e32 v162, s4, v162
	v_lshlrev_b32_e32 v1, 4, v1
	s_movk_i32 s3, 0x3e00
	v_lshrrev_b32_e32 v0, 3, v0
	v_lshl_or_b32 v158, v182, 9, v172
	v_cvt_f16_f32_e32 v5, v5
	v_lshlrev_b64 v[178:179], 9, v[180:181]
	v_or3_b32 v180, s2, v162, v183
	v_and_or_b32 v165, v1, s3, v172
	v_and_or_b32 v0, v0, 32, s4
	ds_write_b16 v159, v2 offset:12352
	ds_write_b16 v159, v3 offset:13376
	ds_write_b16 v159, v4 offset:14400
	ds_write_b16 v159, v5 offset:15424
	s_waitcnt vmcnt(0) lgkmcnt(0)
	s_barrier
	ds_read_b128 v[2:5], v158
	ds_read_b128 v[6:9], v165
	ds_read_b128 v[10:13], v164
	ds_read_b128 v[14:17], v184
	v_lshlrev_b64 v[162:163], 9, v[180:181]
	v_or3_b32 v180, s2, v0, v183
	v_lshlrev_b64 v[0:1], 9, v[180:181]
	v_lshl_add_u64 v[0:1], s[0:1], 0, v[0:1]
	v_lshl_add_u64 v[178:179], s[0:1], 0, v[178:179]
	v_lshl_add_u64 v[162:163], s[0:1], 0, v[162:163]
	v_lshl_add_u64 v[0:1], v[0:1], 0, v[172:173]
	v_lshl_add_u64 v[178:179], v[178:179], 0, v[172:173]
	v_lshl_add_u64 v[162:163], v[162:163], 0, v[172:173]
	s_waitcnt lgkmcnt(3)
	global_store_dwordx4 v[0:1], v[2:5], off sc0 sc1
	s_waitcnt lgkmcnt(2)
	global_store_dwordx4 v[162:163], v[6:9], off sc0 sc1
	s_waitcnt lgkmcnt(1)
	global_store_dwordx4 v[178:179], v[10:13], off sc0 sc1
	s_waitcnt lgkmcnt(0)
	global_store_dwordx4 v[170:171], v[14:17], off sc0 sc1
	s_endpgm
	s_endpgm
	s_endpgm
	s_endpgm
	s_endpgm
	s_endpgm
	s_endpgm
	s_endpgm
	s_endpgm
	s_endpgm
	s_endpgm
	s_endpgm
	s_endpgm
	s_endpgm
	s_endpgm
	s_endpgm
	s_endpgm
	s_endpgm
	s_endpgm
	s_endpgm
	s_endpgm
	s_endpgm
	s_endpgm
	s_endpgm
	s_endpgm
	s_endpgm
	s_endpgm
	s_endpgm
	s_endpgm
	s_endpgm
	s_endpgm
	s_endpgm
	s_endpgm
	s_endpgm
	s_endpgm
	s_endpgm
	s_endpgm
	s_endpgm
	s_endpgm
	s_endpgm
	s_endpgm
	s_endpgm
	s_endpgm
	s_endpgm
	s_endpgm
	s_endpgm
	s_endpgm
	s_endpgm
	s_endpgm
	s_endpgm
	s_endpgm
	s_endpgm
	s_endpgm
	s_endpgm
	s_endpgm
	s_endpgm

.LBB11_10:
	s_or_b64 exec, exec, s[6:7]
	s_waitcnt vmcnt(0) lgkmcnt(0)
	s_barrier
	s_and_saveexec_b64 s[0:1], vcc
	s_cbranch_execz .LBB11_12
	v_lshlrev_b32_e32 v1, 1, v1
	v_lshl_add_u32 v1, v94, 1, v1
	v_bfe_u32 v66, v75, 4, 3
	v_lshl_or_b32 v80, v100, 12, v1
	s_lshl_b64 s[4:5], s[4:5], 8
	s_lshl_b32 s6, s16, 6
	s_lshl_b32 s0, s14, 1
	v_lshrrev_b32_e32 v1, 4, v75
	v_lshl_or_b32 v76, s15, 3, v66
	v_and_b32_e32 v66, 0x78, v99
	v_lshrrev_b32_e32 v0, 3, v0
	s_add_u32 s0, s2, s0
	v_lshlrev_b32_e32 v1, 8, v1
	v_lshlrev_b32_e32 v66, 1, v66
	s_mov_b32 s2, 0x10000
	v_and_or_b32 v0, v0, 16, s6
	v_or3_b32 v81, v1, v66, s2
	v_or3_b32 v0, s4, v0, v76
	v_mov_b32_e32 v1, s5
	v_lshlrev_b64 v[68:69], 9, v[0:1]
	v_or_b32_e32 v0, 0x100, v75
	v_lshlrev_b32_e32 v70, 4, v0
	v_and_b32_e32 v70, 0x1f00, v70
	v_lshrrev_b32_e32 v0, 3, v0
	v_or3_b32 v75, v70, v66, s2
	ds_read_b128 v[70:73], v74
	v_and_or_b32 v0, v0, 48, s6
	v_or3_b32 v0, s4, v0, v76
	ds_read_b128 v[76:79], v74 offset:4096
	s_addc_u32 s1, s3, 0
	s_waitcnt lgkmcnt(1)
	v_add_f32_e32 v70, v50, v70
	v_add_f32_e32 v71, v51, v71
	v_add_f32_e32 v72, v52, v72
	v_add_f32_e32 v73, v53, v73
	ds_read_b128 v[50:53], v74 offset:8192
	s_waitcnt lgkmcnt(1)
	v_add_f32_e32 v76, v54, v76
	v_add_f32_e32 v77, v55, v77
	v_add_f32_e32 v78, v56, v78
	v_add_f32_e32 v79, v57, v79
	ds_read_b128 v[54:57], v74 offset:12288
	s_waitcnt lgkmcnt(1)
	v_add_f32_e32 v58, v58, v50
	v_add_f32_e32 v59, v59, v51
	v_add_f32_e32 v60, v60, v52
	v_add_f32_e32 v61, v61, v53
	ds_read_b128 v[50:53], v74 offset:16384
	s_waitcnt lgkmcnt(1)
	v_add_f32_e32 v62, v62, v54
	v_add_f32_e32 v63, v63, v55
	v_add_f32_e32 v64, v64, v56
	v_add_f32_e32 v65, v65, v57
	ds_read_b128 v[54:57], v74 offset:20480
	s_waitcnt lgkmcnt(1)
	v_add_f32_e32 v50, v34, v50
	v_add_f32_e32 v51, v35, v51
	v_add_f32_e32 v52, v36, v52
	v_add_f32_e32 v53, v37, v53
	ds_read_b128 v[34:37], v74 offset:24576
	s_waitcnt lgkmcnt(1)
	v_add_f32_e32 v54, v38, v54
	v_add_f32_e32 v55, v39, v55
	v_add_f32_e32 v56, v40, v56
	v_add_f32_e32 v57, v41, v57
	ds_read_b128 v[38:41], v74 offset:28672
	s_waitcnt lgkmcnt(1)
	v_add_f32_e32 v42, v42, v34
	v_add_f32_e32 v43, v43, v35
	v_add_f32_e32 v44, v44, v36
	v_add_f32_e32 v45, v45, v37
	ds_read_b128 v[34:37], v74 offset:32768
	s_waitcnt lgkmcnt(1)
	v_add_f32_e32 v46, v46, v38
	v_add_f32_e32 v47, v47, v39
	v_add_f32_e32 v48, v48, v40
	v_add_f32_e32 v49, v49, v41
	ds_read_b128 v[38:41], v74 offset:36864
	s_waitcnt lgkmcnt(1)
	v_add_f32_e32 v34, v18, v34
	v_add_f32_e32 v35, v19, v35
	v_add_f32_e32 v36, v20, v36
	v_add_f32_e32 v37, v21, v37
	ds_read_b128 v[18:21], v74 offset:40960
	s_waitcnt lgkmcnt(1)
	v_add_f32_e32 v38, v22, v38
	v_add_f32_e32 v39, v23, v39
	v_add_f32_e32 v40, v24, v40
	v_add_f32_e32 v41, v25, v41
	ds_read_b128 v[22:25], v74 offset:45056
	s_waitcnt lgkmcnt(1)
	v_add_f32_e32 v26, v26, v18
	v_add_f32_e32 v27, v27, v19
	v_add_f32_e32 v28, v28, v20
	v_add_f32_e32 v29, v29, v21
	ds_read_b128 v[18:21], v74 offset:49152
	s_waitcnt lgkmcnt(1)
	v_add_f32_e32 v30, v30, v22
	v_add_f32_e32 v31, v31, v23
	v_add_f32_e32 v32, v32, v24
	v_add_f32_e32 v33, v33, v25
	ds_read_b128 v[22:25], v74 offset:53248
	s_waitcnt lgkmcnt(1)
	v_add_f32_e32 v18, v2, v18
	v_add_f32_e32 v19, v3, v19
	v_add_f32_e32 v20, v4, v20
	v_add_f32_e32 v21, v5, v21
	ds_read_b128 v[2:5], v74 offset:57344
	s_waitcnt lgkmcnt(1)
	v_add_f32_e32 v22, v6, v22
	v_add_f32_e32 v23, v7, v23
	v_add_f32_e32 v24, v8, v24
	v_add_f32_e32 v25, v9, v25
	ds_read_b128 v[6:9], v74 offset:61440
	s_waitcnt lgkmcnt(1)
	v_add_f32_e32 v2, v10, v2
	v_add_f32_e32 v3, v11, v3
	v_add_f32_e32 v4, v12, v4
	v_add_f32_e32 v5, v13, v5
	v_fma_f32 v10, v96, v70, v95
	v_fma_f32 v11, v96, v71, v95
	v_fma_f32 v12, v96, v72, v95
	v_fma_f32 v13, v96, v73, v95
	s_waitcnt lgkmcnt(0)
	v_add_f32_e32 v6, v14, v6
	v_add_f32_e32 v7, v15, v7
	v_max_f32_e32 v10, v10, v11
	v_max_f32_e32 v11, v12, v13
	v_fma_f32 v12, v96, v76, v95
	v_fma_f32 v13, v96, v77, v95
	v_fma_f32 v14, v96, v78, v95
	v_fma_f32 v15, v96, v79, v95
	v_max3_f32 v10, v10, v11, 0
	v_max_f32_e32 v12, v12, v13
	v_max_f32_e32 v13, v14, v15
	v_cvt_f16_f32_e32 v10, v10
	v_max3_f32 v12, v12, v13, 0
	v_cvt_f16_f32_e32 v12, v12
	v_lshl_add_u32 v11, v98, 8, v80
	v_or_b32_e32 v13, 0x10000, v11
	ds_write_b16 v13, v10
	v_add_u32_e32 v10, 0x10200, v11
	ds_write_b16 v10, v12
	v_fma_f32 v10, v96, v58, v95
	v_fma_f32 v12, v96, v59, v95
	v_fma_f32 v13, v96, v60, v95
	v_fma_f32 v14, v96, v61, v95
	v_max_f32_e32 v10, v10, v12
	v_max_f32_e32 v12, v13, v14
	v_max3_f32 v10, v10, v12, 0
	v_fma_f32 v12, v96, v62, v95
	v_fma_f32 v13, v96, v63, v95
	v_fma_f32 v14, v96, v64, v95
	v_fma_f32 v15, v96, v65, v95
	v_max_f32_e32 v12, v12, v13
	v_max_f32_e32 v13, v14, v15
	v_cvt_f16_f32_e32 v10, v10
	v_max3_f32 v12, v12, v13, 0
	v_cvt_f16_f32_e32 v12, v12
	v_or_b32_e32 v13, 0x10400, v11
	ds_write_b16 v13, v10
	v_add_u32_e32 v10, 0x10600, v11
	ds_write_b16 v10, v12
	v_fma_f32 v10, v96, v34, v95
	v_fma_f32 v12, v96, v35, v95
	v_fma_f32 v13, v96, v36, v95
	v_fma_f32 v14, v96, v37, v95
	v_max_f32_e32 v10, v10, v12
	v_max_f32_e32 v12, v13, v14
	v_max3_f32 v10, v10, v12, 0
	v_fma_f32 v12, v96, v38, v95
	v_fma_f32 v13, v96, v39, v95
	v_fma_f32 v14, v96, v40, v95
	v_fma_f32 v15, v96, v41, v95
	v_max_f32_e32 v12, v12, v13
	v_max_f32_e32 v13, v14, v15
	v_cvt_f16_f32_e32 v10, v10
	v_max3_f32 v12, v12, v13, 0
	v_cvt_f16_f32_e32 v12, v12
	v_or_b32_e32 v13, 0x10800, v11
	ds_write_b16 v13, v10
	v_add_u32_e32 v10, 0x10a00, v11
	ds_write_b16 v10, v12
	v_fma_f32 v10, v96, v26, v95
	v_fma_f32 v12, v96, v27, v95
	v_fma_f32 v13, v96, v28, v95
	v_fma_f32 v14, v96, v29, v95
	v_max_f32_e32 v10, v10, v12
	v_max_f32_e32 v12, v13, v14
	v_max3_f32 v10, v10, v12, 0
	v_fma_f32 v12, v96, v30, v95
	v_fma_f32 v13, v96, v31, v95
	v_fma_f32 v14, v96, v32, v95
	v_fmac_f32_e32 v95, v96, v33
	v_max_f32_e32 v12, v12, v13
	v_max_f32_e32 v13, v14, v95
	v_cvt_f16_f32_e32 v10, v10
	v_max3_f32 v12, v12, v13, 0
	v_cvt_f16_f32_e32 v12, v12
	v_or_b32_e32 v13, 0x10c00, v11
	ds_write_b16 v13, v10
	v_add_u32_e32 v10, 0x10e00, v11
	ds_write_b16 v10, v12
	v_fma_f32 v10, v93, v50, v92
	v_fma_f32 v12, v93, v51, v92
	v_fma_f32 v13, v93, v52, v92
	v_fma_f32 v14, v93, v53, v92
	v_max_f32_e32 v10, v10, v12
	v_max_f32_e32 v12, v13, v14
	v_max3_f32 v10, v10, v12, 0
	v_fma_f32 v12, v93, v54, v92
	v_fma_f32 v13, v93, v55, v92
	v_fma_f32 v14, v93, v56, v92
	v_fma_f32 v15, v93, v57, v92
	v_max_f32_e32 v12, v12, v13
	v_max_f32_e32 v13, v14, v15
	v_cvt_f16_f32_e32 v10, v10
	v_max3_f32 v12, v12, v13, 0
	v_cvt_f16_f32_e32 v12, v12
	v_add_u32_e32 v13, 0x10040, v11
	ds_write_b16 v13, v10
	v_add_u32_e32 v10, 0x10240, v11
	ds_write_b16 v10, v12
	v_fma_f32 v10, v93, v42, v92
	v_fma_f32 v12, v93, v43, v92
	v_fma_f32 v13, v93, v44, v92
	v_fma_f32 v14, v93, v45, v92
	v_max_f32_e32 v10, v10, v12
	v_max_f32_e32 v12, v13, v14
	v_max3_f32 v10, v10, v12, 0
	v_fma_f32 v12, v93, v46, v92
	v_fma_f32 v13, v93, v47, v92
	v_fma_f32 v14, v93, v48, v92
	v_fma_f32 v15, v93, v49, v92
	v_max_f32_e32 v12, v12, v13
	v_max_f32_e32 v13, v14, v15
	v_cvt_f16_f32_e32 v10, v10
	v_max3_f32 v12, v12, v13, 0
	v_cvt_f16_f32_e32 v12, v12
	v_add_u32_e32 v13, 0x10440, v11
	ds_write_b16 v13, v10
	v_add_u32_e32 v10, 0x10640, v11
	ds_write_b16 v10, v12
	v_fma_f32 v10, v93, v18, v92
	v_fma_f32 v12, v93, v19, v92
	v_fma_f32 v13, v93, v20, v92
	v_fma_f32 v14, v93, v21, v92
	v_fma_f32 v2, v93, v2, v92
	v_fma_f32 v3, v93, v3, v92
	v_fma_f32 v4, v93, v4, v92
	v_fma_f32 v5, v93, v5, v92
	v_add_f32_e32 v8, v16, v8
	v_add_f32_e32 v9, v17, v9
	v_max_f32_e32 v10, v10, v12
	v_max_f32_e32 v12, v13, v14
	v_max_f32_e32 v2, v2, v3
	v_max_f32_e32 v3, v4, v5
	v_max3_f32 v10, v10, v12, 0
	v_fma_f32 v12, v93, v22, v92
	v_fma_f32 v13, v93, v23, v92
	v_fma_f32 v14, v93, v24, v92
	v_fma_f32 v15, v93, v25, v92
	v_max3_f32 v2, v2, v3, 0
	v_fma_f32 v3, v93, v6, v92
	v_fma_f32 v4, v93, v7, v92
	v_fma_f32 v5, v93, v8, v92
	v_fmac_f32_e32 v92, v93, v9
	v_max_f32_e32 v12, v12, v13
	v_max_f32_e32 v13, v14, v15
	v_max_f32_e32 v3, v3, v4
	v_max_f32_e32 v4, v5, v92
	v_cvt_f16_f32_e32 v10, v10
	v_max3_f32 v12, v12, v13, 0
	v_cvt_f16_f32_e32 v2, v2
	v_max3_f32 v3, v3, v4, 0
	v_cvt_f16_f32_e32 v12, v12
	v_cvt_f16_f32_e32 v3, v3
	v_add_u32_e32 v13, 0x10840, v11
	v_add_u32_e32 v4, 0x10c40, v11
	ds_write_b16 v13, v10
	v_add_u32_e32 v10, 0x10a40, v11
	ds_write_b16 v4, v2
	v_add_u32_e32 v2, 0x10e40, v11
	ds_write_b16 v10, v12
	ds_write_b16 v2, v3
	s_waitcnt lgkmcnt(0)
	s_barrier
	ds_read_b128 v[2:5], v81
	ds_read_b128 v[6:9], v75
	v_lshl_add_u64 v[68:69], s[0:1], 0, v[68:69]
	v_mov_b32_e32 v67, 0
	v_lshlrev_b64 v[0:1], 9, v[0:1]
	v_lshl_add_u64 v[68:69], v[68:69], 0, v[66:67]
	v_lshl_add_u64 v[0:1], s[0:1], 0, v[0:1]
	v_lshl_add_u64 v[0:1], v[0:1], 0, v[66:67]
	s_waitcnt lgkmcnt(1)
	global_store_dwordx4 v[68:69], v[2:5], off sc0 sc1
	s_waitcnt lgkmcnt(0)
	global_store_dwordx4 v[0:1], v[6:9], off sc0 sc1
